# v64 + grid barrier: the agent-scope acquire's buffer_inv sc1 is issued right after the workgroup's arrival atomic (overlapping the wait / the leader's L2 write-back) instead of after the release is ob
# speedup vs baseline: 1.0077x; 1.0066x over previous
; __device__ __forceinline__ unsigned xb_add(unsigned* p, unsigned v) { return __hip_atomic_fetch_add(p, v, __ATOMIC_RELAXED, __HIP_MEMORY_SCOPE_AGENT); }
; __device__ __forceinline__ void xcd_barrier(const XcdBarrier& b) {
;     ...
;         unsigned nloc = b.st[0], nx = b.st[1];
;         if (nloc == 0u) { xcd_barrier_complete(bar, b.x, nloc, nx); b.st[0] = nloc; b.st[1] = nx; }
;         const unsigned old = xb_add(&bar[XB_XSUB(b.x)], 1u);
;         const unsigned gen = old / nloc;
;         if (old + 1u == (gen + 1u) * nloc) {
.LBB0_208:
	s_or_b64 exec, exec, s[12:13]
	buffer_inv sc1
	v_cvt_f32_u32_e32 v5, v3
	s_waitcnt vmcnt(1)
	v_readfirstlane_b32 s2, v4
	v_sub_u32_e32 v4, 0, v3
	v_rcp_iflag_f32_e32 v5, v5
	v_add_u32_e32 v6, s2, v2
	v_mul_f32_e32 v5, 0x4f7ffffe, v5
	v_cvt_u32_f32_e32 v5, v5
	v_mul_lo_u32 v2, v4, v5
	v_mul_hi_u32 v2, v5, v2
	v_add_u32_e32 v2, v5, v2
	v_mul_hi_u32 v2, v6, v2
	v_mul_lo_u32 v4, v2, v3
	v_sub_u32_e32 v4, v6, v4
	v_add_u32_e32 v5, 1, v2
	v_cmp_ge_u32_e32 vcc, v4, v3
	s_nop 1
	v_cndmask_b32_e32 v2, v2, v5, vcc
	v_sub_u32_e32 v5, v4, v3
	v_cndmask_b32_e32 v4, v4, v5, vcc
	v_add_u32_e32 v5, 1, v2
	v_cmp_ge_u32_e32 vcc, v4, v3
	v_add_u32_e32 v4, 1, v6
	s_nop 0
	v_cndmask_b32_e32 v2, v2, v5, vcc
	v_mul_lo_u32 v5, v3, v2
	v_add_u32_e32 v3, v5, v3
	v_cmp_ne_u32_e32 vcc, v4, v3
	s_and_saveexec_b64 s[2:3], vcc
	s_xor_b64 s[10:11], exec, s[2:3]
	s_cbranch_execz .LBB0_222
	s_waitcnt lgkmcnt(0)
	v_mov_b32_e32 v1, 0x2000
	global_load_dword v1, v1, s[6:7] offset:1024 sc1
	s_add_u32 s14, s6, 0x2400
	s_addc_u32 s15, s7, 0
	s_waitcnt vmcnt(0)
	v_cmp_eq_u32_e32 vcc, v1, v2
	s_and_saveexec_b64 s[12:13], vcc
	s_cbranch_execz .LBB0_221
	s_mov_b32 s2, 1
	s_mov_b64 s[16:17], 0
	v_mov_b32_e32 v1, 0
	s_branch .LBB0_212

; __device__ __forceinline__ unsigned xb_ld(unsigned* p)              { return __hip_atomic_load(p, __ATOMIC_RELAXED, __HIP_MEMORY_SCOPE_AGENT); }
; __device__ __forceinline__ unsigned xb_add(unsigned* p, unsigned v) { return __hip_atomic_fetch_add(p, v, __ATOMIC_RELAXED, __HIP_MEMORY_SCOPE_AGENT); }
; #define XB_SPIN(cond, bar) do { unsigned _sp = 0; while (cond) { __builtin_amdgcn_s_sleep(1); \
;     if ((++_sp & 255u) == 0u) { if (xb_ld(&(bar)[XB_TMO])) break; if (_sp > XB_SPIN_CAP) { atomicAdd(&(bar)[XB_TMO], 1u); break; } } } } while (0)
; __device__ __forceinline__ void xcd_barrier(const XcdBarrier& b) {
;     ...
;         if (old + 1u == (gen + 1u) * nloc) {
;             __builtin_amdgcn_fence(__ATOMIC_RELEASE, "agent");
;             asm volatile("s_waitcnt vmcnt(0)" ::: "memory");
;             const unsigned og = xb_add(&bar[XB_TOP], 1u);
;             const unsigned tg = og / nx;
;             if (og + 1u == (tg + 1u) * nx) xb_add(&bar[XB_TOPGEN], 1u);
;             else XB_SPIN(xb_ld(&bar[XB_TOPGEN]) == tg, bar);
;             __builtin_amdgcn_fence(__ATOMIC_ACQUIRE, "agent");
;             xb_add(&bar[XB_XGEN(b.x)], 1u);
;             asm volatile("s_waitcnt vmcnt(0)" ::: "memory");
;         } else {
;             XB_SPIN(xb_ld(&bar[XB_XGEN(b.x)]) == gen, bar);
;             __builtin_amdgcn_fence(__ATOMIC_ACQUIRE, "agent");
;             asm volatile("s_waitcnt vmcnt(0)" ::: "memory");
;         }
.LBB0_221:
	s_or_b64 exec, exec, s[12:13]
	s_waitcnt vmcnt(0)
.LBB0_222:
	s_andn2_saveexec_b64 s[2:3], s[10:11]
	s_cbranch_execz .LBB0_242
	s_mov_b64 s[10:11], exec
	buffer_wbl2 sc1
	s_waitcnt lgkmcnt(0)
	s_waitcnt vmcnt(0)
	v_mbcnt_lo_u32_b32 v2, s10, 0
	v_mbcnt_hi_u32_b32 v2, s11, v2
	v_cmp_eq_u32_e32 vcc, 0, v2
	s_and_saveexec_b64 s[12:13], vcc
	s_cbranch_execz .LBB0_225
	s_bcnt1_i32_b64 s2, s[10:11]
	v_mov_b32_e32 v3, 0x3000
	v_mov_b32_e32 v4, s2
	global_atomic_add v3, v3, v4, s[90:91] offset:1024 sc0

; __device__ __forceinline__ unsigned xb_add(unsigned* p, unsigned v) { return __hip_atomic_fetch_add(p, v, __ATOMIC_RELAXED, __HIP_MEMORY_SCOPE_AGENT); }
; __device__ __forceinline__ void xcd_barrier(const XcdBarrier& b) {
;     ...
;             __builtin_amdgcn_fence(__ATOMIC_ACQUIRE, "agent");
;             xb_add(&bar[XB_XGEN(b.x)], 1u);
;             asm volatile("s_waitcnt vmcnt(0)" ::: "memory");
.LBB0_239:
	s_or_b64 exec, exec, s[10:11]
	s_mov_b64 s[10:11], exec
	v_mbcnt_lo_u32_b32 v1, s10, 0
	v_mbcnt_hi_u32_b32 v1, s11, v1
	v_cmp_eq_u32_e32 vcc, 0, v1
	s_waitcnt vmcnt(0)
	s_and_saveexec_b64 s[12:13], vcc
	s_cbranch_execz .LBB0_241
	s_bcnt1_i32_b64 s2, s[10:11]
	v_mov_b32_e32 v1, 0x2000
	v_mov_b32_e32 v2, s2
	global_atomic_add v1, v2, s[6:7] offset:1024

; __device__ __forceinline__ unsigned xb_add(unsigned* p, unsigned v) { return __hip_atomic_fetch_add(p, v, __ATOMIC_RELAXED, __HIP_MEMORY_SCOPE_AGENT); }
; __device__ __forceinline__ void xcd_barrier(const XcdBarrier& b) {
;     ...
;         unsigned nloc = b.st[0], nx = b.st[1];
;         if (nloc == 0u) { xcd_barrier_complete(bar, b.x, nloc, nx); b.st[0] = nloc; b.st[1] = nx; }
;         const unsigned old = xb_add(&bar[XB_XSUB(b.x)], 1u);
;         const unsigned gen = old / nloc;
;         if (old + 1u == (gen + 1u) * nloc) {
.LBB0_353:
	s_or_b64 exec, exec, s[10:11]
	buffer_inv sc1
	v_cvt_f32_u32_e32 v5, v3
	s_waitcnt vmcnt(1)
	v_readfirstlane_b32 s2, v4
	v_sub_u32_e32 v4, 0, v3
	v_rcp_iflag_f32_e32 v5, v5
	v_add_u32_e32 v6, s2, v2
	v_mul_f32_e32 v5, 0x4f7ffffe, v5
	v_cvt_u32_f32_e32 v5, v5
	v_mul_lo_u32 v2, v4, v5
	v_mul_hi_u32 v2, v5, v2
	v_add_u32_e32 v2, v5, v2
	v_mul_hi_u32 v2, v6, v2
	v_mul_lo_u32 v4, v2, v3
	v_sub_u32_e32 v4, v6, v4
	v_add_u32_e32 v5, 1, v2
	v_cmp_ge_u32_e32 vcc, v4, v3
	s_nop 1
	v_cndmask_b32_e32 v2, v2, v5, vcc
	v_sub_u32_e32 v5, v4, v3
	v_cndmask_b32_e32 v4, v4, v5, vcc
	v_add_u32_e32 v5, 1, v2
	v_cmp_ge_u32_e32 vcc, v4, v3
	v_add_u32_e32 v4, 1, v6
	s_nop 0
	v_cndmask_b32_e32 v2, v2, v5, vcc
	v_mul_lo_u32 v5, v3, v2
	v_add_u32_e32 v3, v5, v3
	v_cmp_ne_u32_e32 vcc, v4, v3
	s_and_saveexec_b64 s[2:3], vcc
	s_xor_b64 s[8:9], exec, s[2:3]
	s_cbranch_execz .LBB0_367
	s_waitcnt lgkmcnt(0)
	v_mov_b32_e32 v1, 0x2000
	global_load_dword v1, v1, s[6:7] offset:1024 sc1
	s_add_u32 s12, s6, 0x2400
	s_addc_u32 s13, s7, 0
	s_waitcnt vmcnt(0)
	v_cmp_eq_u32_e32 vcc, v1, v2
	s_and_saveexec_b64 s[10:11], vcc
	s_cbranch_execz .LBB0_366
	s_mov_b32 s2, 1
	s_mov_b64 s[14:15], 0
	v_mov_b32_e32 v1, 0
	s_branch .LBB0_357

; __device__ __forceinline__ unsigned xb_ld(unsigned* p)              { return __hip_atomic_load(p, __ATOMIC_RELAXED, __HIP_MEMORY_SCOPE_AGENT); }
; __device__ __forceinline__ unsigned xb_add(unsigned* p, unsigned v) { return __hip_atomic_fetch_add(p, v, __ATOMIC_RELAXED, __HIP_MEMORY_SCOPE_AGENT); }
; #define XB_SPIN(cond, bar) do { unsigned _sp = 0; while (cond) { __builtin_amdgcn_s_sleep(1); \
;     if ((++_sp & 255u) == 0u) { if (xb_ld(&(bar)[XB_TMO])) break; if (_sp > XB_SPIN_CAP) { atomicAdd(&(bar)[XB_TMO], 1u); break; } } } } while (0)
; __device__ __forceinline__ void xcd_barrier(const XcdBarrier& b) {
;     ...
;         if (old + 1u == (gen + 1u) * nloc) {
;             __builtin_amdgcn_fence(__ATOMIC_RELEASE, "agent");
;             asm volatile("s_waitcnt vmcnt(0)" ::: "memory");
;             const unsigned og = xb_add(&bar[XB_TOP], 1u);
;             const unsigned tg = og / nx;
;             if (og + 1u == (tg + 1u) * nx) xb_add(&bar[XB_TOPGEN], 1u);
;             else XB_SPIN(xb_ld(&bar[XB_TOPGEN]) == tg, bar);
;             __builtin_amdgcn_fence(__ATOMIC_ACQUIRE, "agent");
;             xb_add(&bar[XB_XGEN(b.x)], 1u);
;             asm volatile("s_waitcnt vmcnt(0)" ::: "memory");
;         } else {
;             XB_SPIN(xb_ld(&bar[XB_XGEN(b.x)]) == gen, bar);
;             __builtin_amdgcn_fence(__ATOMIC_ACQUIRE, "agent");
;             asm volatile("s_waitcnt vmcnt(0)" ::: "memory");
;         }
.LBB0_366:
	s_or_b64 exec, exec, s[10:11]
	s_waitcnt vmcnt(0)
.LBB0_367:
	s_andn2_saveexec_b64 s[2:3], s[8:9]
	s_cbranch_execz .LBB0_387
	s_mov_b64 s[8:9], exec
	buffer_wbl2 sc1
	s_waitcnt lgkmcnt(0)
	s_waitcnt vmcnt(0)
	v_mbcnt_lo_u32_b32 v2, s8, 0
	v_mbcnt_hi_u32_b32 v2, s9, v2
	v_cmp_eq_u32_e32 vcc, 0, v2
	s_and_saveexec_b64 s[10:11], vcc
	s_cbranch_execz .LBB0_370
	s_bcnt1_i32_b64 s2, s[8:9]
	v_mov_b32_e32 v3, 0x3000
	v_mov_b32_e32 v4, s2
	global_atomic_add v3, v3, v4, s[90:91] offset:1024 sc0

; __device__ __forceinline__ unsigned xb_add(unsigned* p, unsigned v) { return __hip_atomic_fetch_add(p, v, __ATOMIC_RELAXED, __HIP_MEMORY_SCOPE_AGENT); }
; __device__ __forceinline__ void xcd_barrier(const XcdBarrier& b) {
;     ...
;             __builtin_amdgcn_fence(__ATOMIC_ACQUIRE, "agent");
;             xb_add(&bar[XB_XGEN(b.x)], 1u);
;             asm volatile("s_waitcnt vmcnt(0)" ::: "memory");
.LBB0_384:
	s_or_b64 exec, exec, s[8:9]
	s_mov_b64 s[8:9], exec
	v_mbcnt_lo_u32_b32 v1, s8, 0
	v_mbcnt_hi_u32_b32 v1, s9, v1
	v_cmp_eq_u32_e32 vcc, 0, v1
	s_waitcnt vmcnt(0)
	s_and_saveexec_b64 s[10:11], vcc
	s_cbranch_execz .LBB0_386
	s_bcnt1_i32_b64 s2, s[8:9]
	v_mov_b32_e32 v1, 0x2000
	v_mov_b32_e32 v2, s2
	global_atomic_add v1, v2, s[6:7] offset:1024

; __device__ __forceinline__ unsigned xb_add(unsigned* p, unsigned v) { return __hip_atomic_fetch_add(p, v, __ATOMIC_RELAXED, __HIP_MEMORY_SCOPE_AGENT); }
; __device__ __forceinline__ void xcd_barrier(const XcdBarrier& b) {
;     ...
;         unsigned nloc = b.st[0], nx = b.st[1];
;         if (nloc == 0u) { xcd_barrier_complete(bar, b.x, nloc, nx); b.st[0] = nloc; b.st[1] = nx; }
;         const unsigned old = xb_add(&bar[XB_XSUB(b.x)], 1u);
;         const unsigned gen = old / nloc;
;         if (old + 1u == (gen + 1u) * nloc) {
.LBB0_511:
	s_or_b64 exec, exec, s[8:9]
	buffer_inv sc1
	v_cvt_f32_u32_e32 v5, v3
	s_waitcnt vmcnt(1)
	v_readfirstlane_b32 s2, v4
	v_sub_u32_e32 v4, 0, v3
	v_rcp_iflag_f32_e32 v5, v5
	v_add_u32_e32 v6, s2, v2
	v_mul_f32_e32 v5, 0x4f7ffffe, v5
	v_cvt_u32_f32_e32 v5, v5
	v_mul_lo_u32 v2, v4, v5
	v_mul_hi_u32 v2, v5, v2
	v_add_u32_e32 v2, v5, v2
	v_mul_hi_u32 v2, v6, v2
	v_mul_lo_u32 v4, v2, v3
	v_sub_u32_e32 v4, v6, v4
	v_add_u32_e32 v5, 1, v2
	v_cmp_ge_u32_e32 vcc, v4, v3
	s_nop 1
	v_cndmask_b32_e32 v2, v2, v5, vcc
	v_sub_u32_e32 v5, v4, v3
	v_cndmask_b32_e32 v4, v4, v5, vcc
	v_add_u32_e32 v5, 1, v2
	v_cmp_ge_u32_e32 vcc, v4, v3
	v_add_u32_e32 v4, 1, v6
	s_nop 0
	v_cndmask_b32_e32 v2, v2, v5, vcc
	v_mul_lo_u32 v5, v3, v2
	v_add_u32_e32 v3, v5, v3
	v_cmp_ne_u32_e32 vcc, v4, v3
	s_and_saveexec_b64 s[2:3], vcc
	s_xor_b64 s[6:7], exec, s[2:3]
	s_cbranch_execz .LBB0_525
	s_waitcnt lgkmcnt(0)
	v_mov_b32_e32 v1, 0x2000
	global_load_dword v1, v1, s[4:5] offset:1024 sc1
	s_add_u32 s10, s4, 0x2400
	s_addc_u32 s11, s5, 0
	s_waitcnt vmcnt(0)
	v_cmp_eq_u32_e32 vcc, v1, v2
	s_and_saveexec_b64 s[8:9], vcc
	s_cbranch_execz .LBB0_524
	s_mov_b32 s2, 1
	s_mov_b64 s[12:13], 0
	v_mov_b32_e32 v1, 0
	s_branch .LBB0_515

; __device__ __forceinline__ unsigned xb_ld(unsigned* p)              { return __hip_atomic_load(p, __ATOMIC_RELAXED, __HIP_MEMORY_SCOPE_AGENT); }
; __device__ __forceinline__ unsigned xb_add(unsigned* p, unsigned v) { return __hip_atomic_fetch_add(p, v, __ATOMIC_RELAXED, __HIP_MEMORY_SCOPE_AGENT); }
; #define XB_SPIN(cond, bar) do { unsigned _sp = 0; while (cond) { __builtin_amdgcn_s_sleep(1); \
;     if ((++_sp & 255u) == 0u) { if (xb_ld(&(bar)[XB_TMO])) break; if (_sp > XB_SPIN_CAP) { atomicAdd(&(bar)[XB_TMO], 1u); break; } } } } while (0)
; __device__ __forceinline__ void xcd_barrier(const XcdBarrier& b) {
;     ...
;         if (old + 1u == (gen + 1u) * nloc) {
;             __builtin_amdgcn_fence(__ATOMIC_RELEASE, "agent");
;             asm volatile("s_waitcnt vmcnt(0)" ::: "memory");
;             const unsigned og = xb_add(&bar[XB_TOP], 1u);
;             const unsigned tg = og / nx;
;             if (og + 1u == (tg + 1u) * nx) xb_add(&bar[XB_TOPGEN], 1u);
;             else XB_SPIN(xb_ld(&bar[XB_TOPGEN]) == tg, bar);
;             __builtin_amdgcn_fence(__ATOMIC_ACQUIRE, "agent");
;             xb_add(&bar[XB_XGEN(b.x)], 1u);
;             asm volatile("s_waitcnt vmcnt(0)" ::: "memory");
;         } else {
;             XB_SPIN(xb_ld(&bar[XB_XGEN(b.x)]) == gen, bar);
;             __builtin_amdgcn_fence(__ATOMIC_ACQUIRE, "agent");
;             asm volatile("s_waitcnt vmcnt(0)" ::: "memory");
;         }
.LBB0_524:
	s_or_b64 exec, exec, s[8:9]
	s_waitcnt vmcnt(0)
.LBB0_525:
	s_andn2_saveexec_b64 s[2:3], s[6:7]
	s_cbranch_execz .LBB0_545
	s_mov_b64 s[6:7], exec
	buffer_wbl2 sc1
	s_waitcnt lgkmcnt(0)
	s_waitcnt vmcnt(0)
	v_mbcnt_lo_u32_b32 v2, s6, 0
	v_mbcnt_hi_u32_b32 v2, s7, v2
	v_cmp_eq_u32_e32 vcc, 0, v2
	s_and_saveexec_b64 s[8:9], vcc
	s_cbranch_execz .LBB0_528
	s_bcnt1_i32_b64 s2, s[6:7]
	v_mov_b32_e32 v3, 0x3000
	v_mov_b32_e32 v4, s2
	global_atomic_add v3, v3, v4, s[90:91] offset:1024 sc0

; __device__ __forceinline__ unsigned xb_add(unsigned* p, unsigned v) { return __hip_atomic_fetch_add(p, v, __ATOMIC_RELAXED, __HIP_MEMORY_SCOPE_AGENT); }
; __device__ __forceinline__ void xcd_barrier(const XcdBarrier& b) {
;     ...
;             __builtin_amdgcn_fence(__ATOMIC_ACQUIRE, "agent");
;             xb_add(&bar[XB_XGEN(b.x)], 1u);
;             asm volatile("s_waitcnt vmcnt(0)" ::: "memory");
.LBB0_542:
	s_or_b64 exec, exec, s[6:7]
	s_mov_b64 s[6:7], exec
	v_mbcnt_lo_u32_b32 v1, s6, 0
	v_mbcnt_hi_u32_b32 v1, s7, v1
	v_cmp_eq_u32_e32 vcc, 0, v1
	s_waitcnt vmcnt(0)
	s_and_saveexec_b64 s[8:9], vcc
	s_cbranch_execz .LBB0_544
	s_bcnt1_i32_b64 s2, s[6:7]
	v_mov_b32_e32 v1, 0x2000
	v_mov_b32_e32 v2, s2
	global_atomic_add v1, v2, s[4:5] offset:1024

; __device__ __forceinline__ unsigned xb_ld(unsigned* p)              { return __hip_atomic_load(p, __ATOMIC_RELAXED, __HIP_MEMORY_SCOPE_AGENT); }
; __device__ __forceinline__ unsigned xb_add(unsigned* p, unsigned v) { return __hip_atomic_fetch_add(p, v, __ATOMIC_RELAXED, __HIP_MEMORY_SCOPE_AGENT); }
; #define XB_SPIN(cond, bar) do { unsigned _sp = 0; while (cond) { __builtin_amdgcn_s_sleep(1); \
;     if ((++_sp & 255u) == 0u) { if (xb_ld(&(bar)[XB_TMO])) break; if (_sp > XB_SPIN_CAP) { atomicAdd(&(bar)[XB_TMO], 1u); break; } } } } while (0)
; __device__ __forceinline__ void xcd_barrier(const XcdBarrier& b) {
;     ...
;             else XB_SPIN(xb_ld(&bar[XB_TOPGEN]) == tg, bar);
;             __builtin_amdgcn_fence(__ATOMIC_ACQUIRE, "agent");
;             xb_add(&bar[XB_XGEN(b.x)], 1u);
;             asm volatile("s_waitcnt vmcnt(0)" ::: "memory");
;         } else {
;             XB_SPIN(xb_ld(&bar[XB_XGEN(b.x)]) == gen, bar);
;             __builtin_amdgcn_fence(__ATOMIC_ACQUIRE, "agent");
;             asm volatile("s_waitcnt vmcnt(0)" ::: "memory");
;         }
.LBB0_592:
	s_or_b64 exec, exec, s[10:11]
	s_waitcnt vmcnt(0)
.LBB0_593:
	s_andn2_saveexec_b64 s[2:3], s[8:9]
	s_cbranch_execz .LBB0_613
	s_mov_b64 s[8:9], exec
	buffer_wbl2 sc1
	s_waitcnt lgkmcnt(0)
	s_waitcnt vmcnt(0)
	v_mbcnt_lo_u32_b32 v2, s8, 0
	v_mbcnt_hi_u32_b32 v2, s9, v2
	v_cmp_eq_u32_e32 vcc, 0, v2
	s_and_saveexec_b64 s[10:11], vcc
	s_cbranch_execz .LBB0_596
	s_bcnt1_i32_b64 s2, s[8:9]
	v_mov_b32_e32 v3, 0x3000
	v_mov_b32_e32 v4, s2
	global_atomic_add v3, v3, v4, s[90:91] offset:1024 sc0

; __device__ __forceinline__ unsigned xb_ld(unsigned* p)              { return __hip_atomic_load(p, __ATOMIC_RELAXED, __HIP_MEMORY_SCOPE_AGENT); }
; __device__ __forceinline__ unsigned xb_add(unsigned* p, unsigned v) { return __hip_atomic_fetch_add(p, v, __ATOMIC_RELAXED, __HIP_MEMORY_SCOPE_AGENT); }
; #define XB_SPIN(cond, bar) do { unsigned _sp = 0; while (cond) { __builtin_amdgcn_s_sleep(1); \
;     if ((++_sp & 255u) == 0u) { if (xb_ld(&(bar)[XB_TMO])) break; if (_sp > XB_SPIN_CAP) { atomicAdd(&(bar)[XB_TMO], 1u); break; } } } } while (0)
; __device__ __forceinline__ void xcd_barrier(const XcdBarrier& b) {
;     ...
;             else XB_SPIN(xb_ld(&bar[XB_TOPGEN]) == tg, bar);
;             __builtin_amdgcn_fence(__ATOMIC_ACQUIRE, "agent");
;             xb_add(&bar[XB_XGEN(b.x)], 1u);
;             asm volatile("s_waitcnt vmcnt(0)" ::: "memory");
;         } else {
;             XB_SPIN(xb_ld(&bar[XB_XGEN(b.x)]) == gen, bar);
;             __builtin_amdgcn_fence(__ATOMIC_ACQUIRE, "agent");
;             asm volatile("s_waitcnt vmcnt(0)" ::: "memory");
;         }
.LBB0_689:
	s_or_b64 exec, exec, s[10:11]
	s_waitcnt vmcnt(0)
.LBB0_690:
	s_andn2_saveexec_b64 s[2:3], s[8:9]
	s_cbranch_execz .LBB0_710
	s_mov_b64 s[8:9], exec
	buffer_wbl2 sc1
	s_waitcnt lgkmcnt(0)
	s_waitcnt vmcnt(0)
	v_mbcnt_lo_u32_b32 v2, s8, 0
	v_mbcnt_hi_u32_b32 v2, s9, v2
	v_cmp_eq_u32_e32 vcc, 0, v2
	s_and_saveexec_b64 s[10:11], vcc
	s_cbranch_execz .LBB0_693
	s_bcnt1_i32_b64 s2, s[8:9]
	v_mov_b32_e32 v3, 0x3000
	v_mov_b32_e32 v4, s2
	global_atomic_add v3, v3, v4, s[90:91] offset:1024 sc0

; __device__ __forceinline__ unsigned xb_ld(unsigned* p)              { return __hip_atomic_load(p, __ATOMIC_RELAXED, __HIP_MEMORY_SCOPE_AGENT); }
; __device__ __forceinline__ unsigned xb_add(unsigned* p, unsigned v) { return __hip_atomic_fetch_add(p, v, __ATOMIC_RELAXED, __HIP_MEMORY_SCOPE_AGENT); }
; #define XB_SPIN(cond, bar) do { unsigned _sp = 0; while (cond) { __builtin_amdgcn_s_sleep(1); \
;     if ((++_sp & 255u) == 0u) { if (xb_ld(&(bar)[XB_TMO])) break; if (_sp > XB_SPIN_CAP) { atomicAdd(&(bar)[XB_TMO], 1u); break; } } } } while (0)
; __device__ __forceinline__ void xcd_barrier(const XcdBarrier& b) {
;     ...
;             else XB_SPIN(xb_ld(&bar[XB_TOPGEN]) == tg, bar);
;             __builtin_amdgcn_fence(__ATOMIC_ACQUIRE, "agent");
;             xb_add(&bar[XB_XGEN(b.x)], 1u);
;             asm volatile("s_waitcnt vmcnt(0)" ::: "memory");
;         } else {
;             XB_SPIN(xb_ld(&bar[XB_XGEN(b.x)]) == gen, bar);
;             __builtin_amdgcn_fence(__ATOMIC_ACQUIRE, "agent");
;             asm volatile("s_waitcnt vmcnt(0)" ::: "memory");
;         }
.LBB0_811:
	s_or_b64 exec, exec, s[10:11]
	s_waitcnt vmcnt(0)
.LBB0_812:
	s_andn2_saveexec_b64 s[2:3], s[8:9]
	s_cbranch_execz .LBB0_832
	s_mov_b64 s[8:9], exec
	buffer_wbl2 sc1
	s_waitcnt lgkmcnt(0)
	s_waitcnt vmcnt(0)
	v_mbcnt_lo_u32_b32 v2, s8, 0
	v_mbcnt_hi_u32_b32 v2, s9, v2
	v_cmp_eq_u32_e32 vcc, 0, v2
	s_and_saveexec_b64 s[10:11], vcc
	s_cbranch_execz .LBB0_815
	s_bcnt1_i32_b64 s2, s[8:9]
	v_mov_b32_e32 v3, 0x3000
	v_mov_b32_e32 v4, s2
	global_atomic_add v3, v3, v4, s[90:91] offset:1024 sc0

; __device__ __forceinline__ unsigned xb_ld(unsigned* p)              { return __hip_atomic_load(p, __ATOMIC_RELAXED, __HIP_MEMORY_SCOPE_AGENT); }
; __device__ __forceinline__ unsigned xb_add(unsigned* p, unsigned v) { return __hip_atomic_fetch_add(p, v, __ATOMIC_RELAXED, __HIP_MEMORY_SCOPE_AGENT); }
; #define XB_SPIN(cond, bar) do { unsigned _sp = 0; while (cond) { __builtin_amdgcn_s_sleep(1); \
;     if ((++_sp & 255u) == 0u) { if (xb_ld(&(bar)[XB_TMO])) break; if (_sp > XB_SPIN_CAP) { atomicAdd(&(bar)[XB_TMO], 1u); break; } } } } while (0)
; __device__ __forceinline__ void xcd_barrier(const XcdBarrier& b) {
;     ...
;             else XB_SPIN(xb_ld(&bar[XB_TOPGEN]) == tg, bar);
;             __builtin_amdgcn_fence(__ATOMIC_ACQUIRE, "agent");
;             xb_add(&bar[XB_XGEN(b.x)], 1u);
;             asm volatile("s_waitcnt vmcnt(0)" ::: "memory");
;         } else {
;             XB_SPIN(xb_ld(&bar[XB_XGEN(b.x)]) == gen, bar);
;             __builtin_amdgcn_fence(__ATOMIC_ACQUIRE, "agent");
;             asm volatile("s_waitcnt vmcnt(0)" ::: "memory");
;         }
.LBB0_912:
	s_or_b64 exec, exec, s[8:9]
	s_waitcnt vmcnt(0)
.LBB0_913:
	s_andn2_saveexec_b64 s[2:3], s[6:7]
	s_cbranch_execz .LBB0_933
	s_mov_b64 s[6:7], exec
	buffer_wbl2 sc1
	s_waitcnt lgkmcnt(0)
	s_waitcnt vmcnt(0)
	v_mbcnt_lo_u32_b32 v2, s6, 0
	v_mbcnt_hi_u32_b32 v2, s7, v2
	v_cmp_eq_u32_e32 vcc, 0, v2
	s_and_saveexec_b64 s[8:9], vcc
	s_cbranch_execz .LBB0_916
	s_bcnt1_i32_b64 s2, s[6:7]
	v_mov_b32_e32 v3, 0x3000
	v_mov_b32_e32 v4, s2
	global_atomic_add v3, v3, v4, s[90:91] offset:1024 sc0

; __device__ __forceinline__ unsigned xb_ld(unsigned* p)              { return __hip_atomic_load(p, __ATOMIC_RELAXED, __HIP_MEMORY_SCOPE_AGENT); }
; __device__ __forceinline__ unsigned xb_add(unsigned* p, unsigned v) { return __hip_atomic_fetch_add(p, v, __ATOMIC_RELAXED, __HIP_MEMORY_SCOPE_AGENT); }
; #define XB_SPIN(cond, bar) do { unsigned _sp = 0; while (cond) { __builtin_amdgcn_s_sleep(1); \
;     if ((++_sp & 255u) == 0u) { if (xb_ld(&(bar)[XB_TMO])) break; if (_sp > XB_SPIN_CAP) { atomicAdd(&(bar)[XB_TMO], 1u); break; } } } } while (0)
; __device__ __forceinline__ void xcd_barrier(const XcdBarrier& b) {
;     ...
;             else XB_SPIN(xb_ld(&bar[XB_TOPGEN]) == tg, bar);
;             __builtin_amdgcn_fence(__ATOMIC_ACQUIRE, "agent");
;             xb_add(&bar[XB_XGEN(b.x)], 1u);
;             asm volatile("s_waitcnt vmcnt(0)" ::: "memory");
;         } else {
;             XB_SPIN(xb_ld(&bar[XB_XGEN(b.x)]) == gen, bar);
;             __builtin_amdgcn_fence(__ATOMIC_ACQUIRE, "agent");
;             asm volatile("s_waitcnt vmcnt(0)" ::: "memory");
;         }
.LBB0_1057:
	s_or_b64 exec, exec, s[10:11]
	s_waitcnt vmcnt(0)
.LBB0_1058:
	s_andn2_saveexec_b64 s[2:3], s[8:9]
	s_cbranch_execz .LBB0_1078
	s_mov_b64 s[8:9], exec
	buffer_wbl2 sc1
	s_waitcnt lgkmcnt(0)
	s_waitcnt vmcnt(0)
	v_mbcnt_lo_u32_b32 v2, s8, 0
	v_mbcnt_hi_u32_b32 v2, s9, v2
	v_cmp_eq_u32_e32 vcc, 0, v2
	s_and_saveexec_b64 s[10:11], vcc
	s_cbranch_execz .LBB0_1061
	s_bcnt1_i32_b64 s2, s[8:9]
	v_mov_b32_e32 v3, 0x3000
	v_mov_b32_e32 v4, s2
	global_atomic_add v3, v3, v4, s[90:91] offset:1024 sc0

; __device__ __forceinline__ unsigned xb_ld(unsigned* p)              { return __hip_atomic_load(p, __ATOMIC_RELAXED, __HIP_MEMORY_SCOPE_AGENT); }
; __device__ __forceinline__ unsigned xb_add(unsigned* p, unsigned v) { return __hip_atomic_fetch_add(p, v, __ATOMIC_RELAXED, __HIP_MEMORY_SCOPE_AGENT); }
; #define XB_SPIN(cond, bar) do { unsigned _sp = 0; while (cond) { __builtin_amdgcn_s_sleep(1); \
;     if ((++_sp & 255u) == 0u) { if (xb_ld(&(bar)[XB_TMO])) break; if (_sp > XB_SPIN_CAP) { atomicAdd(&(bar)[XB_TMO], 1u); break; } } } } while (0)
; __device__ __forceinline__ void xcd_barrier(const XcdBarrier& b) {
;     ...
;             else XB_SPIN(xb_ld(&bar[XB_TOPGEN]) == tg, bar);
;             __builtin_amdgcn_fence(__ATOMIC_ACQUIRE, "agent");
;             xb_add(&bar[XB_XGEN(b.x)], 1u);
;             asm volatile("s_waitcnt vmcnt(0)" ::: "memory");
;         } else {
;             XB_SPIN(xb_ld(&bar[XB_XGEN(b.x)]) == gen, bar);
;             __builtin_amdgcn_fence(__ATOMIC_ACQUIRE, "agent");
;             asm volatile("s_waitcnt vmcnt(0)" ::: "memory");
;         }
.LBB0_1215:
	s_or_b64 exec, exec, s[8:9]
	s_waitcnt vmcnt(0)
.LBB0_1216:
	s_andn2_saveexec_b64 s[2:3], s[6:7]
	s_cbranch_execz .LBB0_1236
	s_mov_b64 s[6:7], exec
	buffer_wbl2 sc1
	s_waitcnt lgkmcnt(0)
	s_waitcnt vmcnt(0)
	v_mbcnt_lo_u32_b32 v2, s6, 0
	v_mbcnt_hi_u32_b32 v2, s7, v2
	v_cmp_eq_u32_e32 vcc, 0, v2
	s_and_saveexec_b64 s[8:9], vcc
	s_cbranch_execz .LBB0_1219
	s_bcnt1_i32_b64 s2, s[6:7]
	v_mov_b32_e32 v3, 0x3000
	v_mov_b32_e32 v4, s2
	global_atomic_add v3, v3, v4, s[90:91] offset:1024 sc0

; __device__ __forceinline__ unsigned xb_ld(unsigned* p)              { return __hip_atomic_load(p, __ATOMIC_RELAXED, __HIP_MEMORY_SCOPE_AGENT); }
; __device__ __forceinline__ unsigned xb_add(unsigned* p, unsigned v) { return __hip_atomic_fetch_add(p, v, __ATOMIC_RELAXED, __HIP_MEMORY_SCOPE_AGENT); }
; #define XB_SPIN(cond, bar) do { unsigned _sp = 0; while (cond) { __builtin_amdgcn_s_sleep(1); \
;     if ((++_sp & 255u) == 0u) { if (xb_ld(&(bar)[XB_TMO])) break; if (_sp > XB_SPIN_CAP) { atomicAdd(&(bar)[XB_TMO], 1u); break; } } } } while (0)
; __device__ __forceinline__ void xcd_barrier(const XcdBarrier& b) {
;     ...
;             else XB_SPIN(xb_ld(&bar[XB_TOPGEN]) == tg, bar);
;             __builtin_amdgcn_fence(__ATOMIC_ACQUIRE, "agent");
;             xb_add(&bar[XB_XGEN(b.x)], 1u);
;             asm volatile("s_waitcnt vmcnt(0)" ::: "memory");
;         } else {
;             XB_SPIN(xb_ld(&bar[XB_XGEN(b.x)]) == gen, bar);
;             __builtin_amdgcn_fence(__ATOMIC_ACQUIRE, "agent");
;             asm volatile("s_waitcnt vmcnt(0)" ::: "memory");
;         }
.LBB0_1282:
	s_or_b64 exec, exec, s[10:11]
	s_waitcnt vmcnt(0)
.LBB0_1283:
	s_andn2_saveexec_b64 s[2:3], s[8:9]
	s_cbranch_execz .LBB0_1303
	s_mov_b64 s[8:9], exec
	buffer_wbl2 sc1
	s_waitcnt lgkmcnt(0)
	s_waitcnt vmcnt(0)
	v_mbcnt_lo_u32_b32 v2, s8, 0
	v_mbcnt_hi_u32_b32 v2, s9, v2
	v_cmp_eq_u32_e32 vcc, 0, v2
	s_and_saveexec_b64 s[10:11], vcc
	s_cbranch_execz .LBB0_1286
	s_bcnt1_i32_b64 s2, s[8:9]
	v_mov_b32_e32 v3, 0x3000
	v_mov_b32_e32 v4, s2
	global_atomic_add v3, v3, v4, s[90:91] offset:1024 sc0

; __device__ __forceinline__ unsigned xb_ld(unsigned* p)              { return __hip_atomic_load(p, __ATOMIC_RELAXED, __HIP_MEMORY_SCOPE_AGENT); }
; __device__ __forceinline__ unsigned xb_add(unsigned* p, unsigned v) { return __hip_atomic_fetch_add(p, v, __ATOMIC_RELAXED, __HIP_MEMORY_SCOPE_AGENT); }
; #define XB_SPIN(cond, bar) do { unsigned _sp = 0; while (cond) { __builtin_amdgcn_s_sleep(1); \
;     if ((++_sp & 255u) == 0u) { if (xb_ld(&(bar)[XB_TMO])) break; if (_sp > XB_SPIN_CAP) { atomicAdd(&(bar)[XB_TMO], 1u); break; } } } } while (0)
; __device__ __forceinline__ void xcd_barrier(const XcdBarrier& b) {
;     ...
;             else XB_SPIN(xb_ld(&bar[XB_TOPGEN]) == tg, bar);
;             __builtin_amdgcn_fence(__ATOMIC_ACQUIRE, "agent");
;             xb_add(&bar[XB_XGEN(b.x)], 1u);
;             asm volatile("s_waitcnt vmcnt(0)" ::: "memory");
;         } else {
;             XB_SPIN(xb_ld(&bar[XB_XGEN(b.x)]) == gen, bar);
;             __builtin_amdgcn_fence(__ATOMIC_ACQUIRE, "agent");
;             asm volatile("s_waitcnt vmcnt(0)" ::: "memory");
;         }
.LBB0_1379:
	s_or_b64 exec, exec, s[10:11]
	s_waitcnt vmcnt(0)
.LBB0_1380:
	s_andn2_saveexec_b64 s[2:3], s[8:9]
	s_cbranch_execz .LBB0_1400
	s_mov_b64 s[8:9], exec
	buffer_wbl2 sc1
	s_waitcnt lgkmcnt(0)
	s_waitcnt vmcnt(0)
	v_mbcnt_lo_u32_b32 v2, s8, 0
	v_mbcnt_hi_u32_b32 v2, s9, v2
	v_cmp_eq_u32_e32 vcc, 0, v2
	s_and_saveexec_b64 s[10:11], vcc
	s_cbranch_execz .LBB0_1383
	s_bcnt1_i32_b64 s2, s[8:9]
	v_mov_b32_e32 v3, 0x3000
	v_mov_b32_e32 v4, s2
	global_atomic_add v3, v3, v4, s[90:91] offset:1024 sc0

; __device__ __forceinline__ unsigned xb_ld(unsigned* p)              { return __hip_atomic_load(p, __ATOMIC_RELAXED, __HIP_MEMORY_SCOPE_AGENT); }
; __device__ __forceinline__ unsigned xb_add(unsigned* p, unsigned v) { return __hip_atomic_fetch_add(p, v, __ATOMIC_RELAXED, __HIP_MEMORY_SCOPE_AGENT); }
; #define XB_SPIN(cond, bar) do { unsigned _sp = 0; while (cond) { __builtin_amdgcn_s_sleep(1); \
;     if ((++_sp & 255u) == 0u) { if (xb_ld(&(bar)[XB_TMO])) break; if (_sp > XB_SPIN_CAP) { atomicAdd(&(bar)[XB_TMO], 1u); break; } } } } while (0)
; __device__ __forceinline__ void xcd_barrier(const XcdBarrier& b) {
;     ...
;             else XB_SPIN(xb_ld(&bar[XB_TOPGEN]) == tg, bar);
;             __builtin_amdgcn_fence(__ATOMIC_ACQUIRE, "agent");
;             xb_add(&bar[XB_XGEN(b.x)], 1u);
;             asm volatile("s_waitcnt vmcnt(0)" ::: "memory");
;         } else {
;             XB_SPIN(xb_ld(&bar[XB_XGEN(b.x)]) == gen, bar);
;             __builtin_amdgcn_fence(__ATOMIC_ACQUIRE, "agent");
;             asm volatile("s_waitcnt vmcnt(0)" ::: "memory");
;         }
.LBB0_1471:
	s_or_b64 exec, exec, s[10:11]
	s_waitcnt vmcnt(0)
.LBB0_1472:
	s_andn2_saveexec_b64 s[2:3], s[8:9]
	s_cbranch_execz .LBB0_1492
	s_mov_b64 s[8:9], exec
	buffer_wbl2 sc1
	s_waitcnt lgkmcnt(0)
	s_waitcnt vmcnt(0)
	v_mbcnt_lo_u32_b32 v2, s8, 0
	v_mbcnt_hi_u32_b32 v2, s9, v2
	v_cmp_eq_u32_e32 vcc, 0, v2
	s_and_saveexec_b64 s[10:11], vcc
	s_cbranch_execz .LBB0_1475
	s_bcnt1_i32_b64 s2, s[8:9]
	v_mov_b32_e32 v3, 0x3000
	v_mov_b32_e32 v4, s2
	global_atomic_add v3, v3, v4, s[90:91] offset:1024 sc0

; __device__ __forceinline__ unsigned xb_add(unsigned* p, unsigned v) { return __hip_atomic_fetch_add(p, v, __ATOMIC_RELAXED, __HIP_MEMORY_SCOPE_AGENT); }
; __device__ __forceinline__ void xcd_barrier(const XcdBarrier& b) {
;     ...
;         unsigned nloc = b.st[0], nx = b.st[1];
;         if (nloc == 0u) { xcd_barrier_complete(bar, b.x, nloc, nx); b.st[0] = nloc; b.st[1] = nx; }
;         const unsigned old = xb_add(&bar[XB_XSUB(b.x)], 1u);
;         const unsigned gen = old / nloc;
;         if (old + 1u == (gen + 1u) * nloc) {
.LBB0_1673:
	s_or_b64 exec, exec, s[22:23]
	buffer_inv sc1
	v_cvt_f32_u32_e32 v5, v3
	s_waitcnt vmcnt(1)
	v_readfirstlane_b32 s2, v4
	v_sub_u32_e32 v4, 0, v3
	v_rcp_iflag_f32_e32 v5, v5
	v_add_u32_e32 v6, s2, v2
	v_mul_f32_e32 v5, 0x4f7ffffe, v5
	v_cvt_u32_f32_e32 v5, v5
	v_mul_lo_u32 v2, v4, v5
	v_mul_hi_u32 v2, v5, v2
	v_add_u32_e32 v2, v5, v2
	v_mul_hi_u32 v2, v6, v2
	v_mul_lo_u32 v4, v2, v3
	v_sub_u32_e32 v4, v6, v4
	v_add_u32_e32 v5, 1, v2
	v_cmp_ge_u32_e32 vcc, v4, v3
	s_nop 1
	v_cndmask_b32_e32 v2, v2, v5, vcc
	v_sub_u32_e32 v5, v4, v3
	v_cndmask_b32_e32 v4, v4, v5, vcc
	v_add_u32_e32 v5, 1, v2
	v_cmp_ge_u32_e32 vcc, v4, v3
	v_add_u32_e32 v4, 1, v6
	s_nop 0
	v_cndmask_b32_e32 v2, v2, v5, vcc
	v_mul_lo_u32 v5, v3, v2
	v_add_u32_e32 v3, v5, v3
	v_cmp_ne_u32_e32 vcc, v4, v3
	s_and_saveexec_b64 s[2:3], vcc
	s_xor_b64 s[10:11], exec, s[2:3]
	s_cbranch_execz .LBB0_1687
	s_waitcnt lgkmcnt(0)
	v_mov_b32_e32 v1, 0x2000
	global_load_dword v1, v1, s[8:9] offset:1024 sc1
	s_add_u32 s24, s8, 0x2400
	s_addc_u32 s25, s9, 0
	s_waitcnt vmcnt(0)
	v_cmp_eq_u32_e32 vcc, v1, v2
	s_and_saveexec_b64 s[22:23], vcc
	s_cbranch_execz .LBB0_1686
	s_mov_b32 s2, 1
	s_mov_b64 s[26:27], 0
	v_mov_b32_e32 v1, 0
	s_branch .LBB0_1677

; __device__ __forceinline__ unsigned xb_ld(unsigned* p)              { return __hip_atomic_load(p, __ATOMIC_RELAXED, __HIP_MEMORY_SCOPE_AGENT); }
; __device__ __forceinline__ unsigned xb_add(unsigned* p, unsigned v) { return __hip_atomic_fetch_add(p, v, __ATOMIC_RELAXED, __HIP_MEMORY_SCOPE_AGENT); }
; #define XB_SPIN(cond, bar) do { unsigned _sp = 0; while (cond) { __builtin_amdgcn_s_sleep(1); \
;     if ((++_sp & 255u) == 0u) { if (xb_ld(&(bar)[XB_TMO])) break; if (_sp > XB_SPIN_CAP) { atomicAdd(&(bar)[XB_TMO], 1u); break; } } } } while (0)
; __device__ __forceinline__ void xcd_barrier(const XcdBarrier& b) {
;     ...
;         if (old + 1u == (gen + 1u) * nloc) {
;             __builtin_amdgcn_fence(__ATOMIC_RELEASE, "agent");
;             asm volatile("s_waitcnt vmcnt(0)" ::: "memory");
;             const unsigned og = xb_add(&bar[XB_TOP], 1u);
;             const unsigned tg = og / nx;
;             if (og + 1u == (tg + 1u) * nx) xb_add(&bar[XB_TOPGEN], 1u);
;             else XB_SPIN(xb_ld(&bar[XB_TOPGEN]) == tg, bar);
;             __builtin_amdgcn_fence(__ATOMIC_ACQUIRE, "agent");
;             xb_add(&bar[XB_XGEN(b.x)], 1u);
;             asm volatile("s_waitcnt vmcnt(0)" ::: "memory");
;         } else {
;             XB_SPIN(xb_ld(&bar[XB_XGEN(b.x)]) == gen, bar);
;             __builtin_amdgcn_fence(__ATOMIC_ACQUIRE, "agent");
;             asm volatile("s_waitcnt vmcnt(0)" ::: "memory");
;         }
.LBB0_1686:
	s_or_b64 exec, exec, s[22:23]
	s_waitcnt vmcnt(0)
.LBB0_1687:
	s_andn2_saveexec_b64 s[2:3], s[10:11]
	s_cbranch_execz .LBB0_1707
	s_mov_b64 s[10:11], exec
	buffer_wbl2 sc1
	s_waitcnt lgkmcnt(0)
	s_waitcnt vmcnt(0)
	v_mbcnt_lo_u32_b32 v2, s10, 0
	v_mbcnt_hi_u32_b32 v2, s11, v2
	v_cmp_eq_u32_e32 vcc, 0, v2
	s_and_saveexec_b64 s[22:23], vcc
	s_cbranch_execz .LBB0_1690
	s_bcnt1_i32_b64 s2, s[10:11]
	v_mov_b32_e32 v3, 0x3000
	v_mov_b32_e32 v4, s2
	global_atomic_add v3, v3, v4, s[90:91] offset:1024 sc0

; __device__ __forceinline__ unsigned xb_add(unsigned* p, unsigned v) { return __hip_atomic_fetch_add(p, v, __ATOMIC_RELAXED, __HIP_MEMORY_SCOPE_AGENT); }
; __device__ __forceinline__ void xcd_barrier(const XcdBarrier& b) {
;     ...
;             __builtin_amdgcn_fence(__ATOMIC_ACQUIRE, "agent");
;             xb_add(&bar[XB_XGEN(b.x)], 1u);
;             asm volatile("s_waitcnt vmcnt(0)" ::: "memory");
.LBB0_1704:
	s_or_b64 exec, exec, s[10:11]
	s_mov_b64 s[10:11], exec
	v_mbcnt_lo_u32_b32 v1, s10, 0
	v_mbcnt_hi_u32_b32 v1, s11, v1
	v_cmp_eq_u32_e32 vcc, 0, v1
	s_waitcnt vmcnt(0)
	s_and_saveexec_b64 s[22:23], vcc
	s_cbranch_execz .LBB0_1706
	s_bcnt1_i32_b64 s2, s[10:11]
	v_mov_b32_e32 v1, 0x2000
	v_mov_b32_e32 v2, s2
	global_atomic_add v1, v2, s[8:9] offset:1024

; __device__ __forceinline__ unsigned xb_add(unsigned* p, unsigned v) { return __hip_atomic_fetch_add(p, v, __ATOMIC_RELAXED, __HIP_MEMORY_SCOPE_AGENT); }
; __device__ __forceinline__ void xcd_barrier(const XcdBarrier& b) {
;     ...
;         unsigned nloc = b.st[0], nx = b.st[1];
;         if (nloc == 0u) { xcd_barrier_complete(bar, b.x, nloc, nx); b.st[0] = nloc; b.st[1] = nx; }
;         const unsigned old = xb_add(&bar[XB_XSUB(b.x)], 1u);
;         const unsigned gen = old / nloc;
;         if (old + 1u == (gen + 1u) * nloc) {
.LBB0_1766:
	s_or_b64 exec, exec, s[10:11]
	buffer_inv sc1
	v_cvt_f32_u32_e32 v5, v3
	s_waitcnt vmcnt(1)
	v_readfirstlane_b32 s2, v4
	v_sub_u32_e32 v4, 0, v3
	v_rcp_iflag_f32_e32 v5, v5
	v_add_u32_e32 v6, s2, v2
	v_mul_f32_e32 v5, 0x4f7ffffe, v5
	v_cvt_u32_f32_e32 v5, v5
	v_mul_lo_u32 v2, v4, v5
	v_mul_hi_u32 v2, v5, v2
	v_add_u32_e32 v2, v5, v2
	v_mul_hi_u32 v2, v6, v2
	v_mul_lo_u32 v4, v2, v3
	v_sub_u32_e32 v4, v6, v4
	v_add_u32_e32 v5, 1, v2
	v_cmp_ge_u32_e32 vcc, v4, v3
	s_nop 1
	v_cndmask_b32_e32 v2, v2, v5, vcc
	v_sub_u32_e32 v5, v4, v3
	v_cndmask_b32_e32 v4, v4, v5, vcc
	v_add_u32_e32 v5, 1, v2
	v_cmp_ge_u32_e32 vcc, v4, v3
	v_add_u32_e32 v4, 1, v6
	s_nop 0
	v_cndmask_b32_e32 v2, v2, v5, vcc
	v_mul_lo_u32 v5, v3, v2
	v_add_u32_e32 v3, v5, v3
	v_cmp_ne_u32_e32 vcc, v4, v3
	s_and_saveexec_b64 s[2:3], vcc
	s_xor_b64 s[8:9], exec, s[2:3]
	s_cbranch_execz .LBB0_1780
	s_waitcnt lgkmcnt(0)
	v_mov_b32_e32 v1, 0x2000
	global_load_dword v1, v1, s[6:7] offset:1024 sc1
	s_add_u32 s18, s6, 0x2400
	s_addc_u32 s19, s7, 0
	s_waitcnt vmcnt(0)
	v_cmp_eq_u32_e32 vcc, v1, v2
	s_and_saveexec_b64 s[10:11], vcc
	s_cbranch_execz .LBB0_1779
	s_mov_b32 s2, 1
	s_mov_b64 s[20:21], 0
	v_mov_b32_e32 v1, 0
	s_branch .LBB0_1770

; __device__ __forceinline__ unsigned xb_ld(unsigned* p)              { return __hip_atomic_load(p, __ATOMIC_RELAXED, __HIP_MEMORY_SCOPE_AGENT); }
; __device__ __forceinline__ unsigned xb_add(unsigned* p, unsigned v) { return __hip_atomic_fetch_add(p, v, __ATOMIC_RELAXED, __HIP_MEMORY_SCOPE_AGENT); }
; #define XB_SPIN(cond, bar) do { unsigned _sp = 0; while (cond) { __builtin_amdgcn_s_sleep(1); \
;     if ((++_sp & 255u) == 0u) { if (xb_ld(&(bar)[XB_TMO])) break; if (_sp > XB_SPIN_CAP) { atomicAdd(&(bar)[XB_TMO], 1u); break; } } } } while (0)
; __device__ __forceinline__ void xcd_barrier(const XcdBarrier& b) {
;     ...
;         if (old + 1u == (gen + 1u) * nloc) {
;             __builtin_amdgcn_fence(__ATOMIC_RELEASE, "agent");
;             asm volatile("s_waitcnt vmcnt(0)" ::: "memory");
;             const unsigned og = xb_add(&bar[XB_TOP], 1u);
;             const unsigned tg = og / nx;
;             if (og + 1u == (tg + 1u) * nx) xb_add(&bar[XB_TOPGEN], 1u);
;             else XB_SPIN(xb_ld(&bar[XB_TOPGEN]) == tg, bar);
;             __builtin_amdgcn_fence(__ATOMIC_ACQUIRE, "agent");
;             xb_add(&bar[XB_XGEN(b.x)], 1u);
;             asm volatile("s_waitcnt vmcnt(0)" ::: "memory");
;         } else {
;             XB_SPIN(xb_ld(&bar[XB_XGEN(b.x)]) == gen, bar);
;             __builtin_amdgcn_fence(__ATOMIC_ACQUIRE, "agent");
;             asm volatile("s_waitcnt vmcnt(0)" ::: "memory");
;         }
.LBB0_1779:
	s_or_b64 exec, exec, s[10:11]
	s_waitcnt vmcnt(0)
.LBB0_1780:
	s_andn2_saveexec_b64 s[2:3], s[8:9]
	s_cbranch_execz .LBB0_1800
	s_mov_b64 s[8:9], exec
	buffer_wbl2 sc1
	s_waitcnt lgkmcnt(0)
	s_waitcnt vmcnt(0)
	v_mbcnt_lo_u32_b32 v2, s8, 0
	v_mbcnt_hi_u32_b32 v2, s9, v2
	v_cmp_eq_u32_e32 vcc, 0, v2
	s_and_saveexec_b64 s[10:11], vcc
	s_cbranch_execz .LBB0_1783
	s_bcnt1_i32_b64 s2, s[8:9]
	v_mov_b32_e32 v3, 0x3000
	v_mov_b32_e32 v4, s2
	global_atomic_add v3, v3, v4, s[90:91] offset:1024 sc0

; __device__ __forceinline__ unsigned xb_add(unsigned* p, unsigned v) { return __hip_atomic_fetch_add(p, v, __ATOMIC_RELAXED, __HIP_MEMORY_SCOPE_AGENT); }
; __device__ __forceinline__ void xcd_barrier(const XcdBarrier& b) {
;     ...
;         unsigned nloc = b.st[0], nx = b.st[1];
;         if (nloc == 0u) { xcd_barrier_complete(bar, b.x, nloc, nx); b.st[0] = nloc; b.st[1] = nx; }
;         const unsigned old = xb_add(&bar[XB_XSUB(b.x)], 1u);
;         const unsigned gen = old / nloc;
;         if (old + 1u == (gen + 1u) * nloc) {
.LBB0_1870:
	s_or_b64 exec, exec, s[14:15]
	buffer_inv sc1
	v_cvt_f32_u32_e32 v5, v3
	s_waitcnt vmcnt(1)
	v_readfirstlane_b32 s2, v4
	v_sub_u32_e32 v4, 0, v3
	v_rcp_iflag_f32_e32 v5, v5
	v_add_u32_e32 v6, s2, v2
	v_mul_f32_e32 v5, 0x4f7ffffe, v5
	v_cvt_u32_f32_e32 v5, v5
	v_mul_lo_u32 v2, v4, v5
	v_mul_hi_u32 v2, v5, v2
	v_add_u32_e32 v2, v5, v2
	v_mul_hi_u32 v2, v6, v2
	v_mul_lo_u32 v4, v2, v3
	v_sub_u32_e32 v4, v6, v4
	v_add_u32_e32 v5, 1, v2
	v_cmp_ge_u32_e32 vcc, v4, v3
	s_nop 1
	v_cndmask_b32_e32 v2, v2, v5, vcc
	v_sub_u32_e32 v5, v4, v3
	v_cndmask_b32_e32 v4, v4, v5, vcc
	v_add_u32_e32 v5, 1, v2
	v_cmp_ge_u32_e32 vcc, v4, v3
	v_add_u32_e32 v4, 1, v6
	s_nop 0
	v_cndmask_b32_e32 v2, v2, v5, vcc
	v_mul_lo_u32 v5, v3, v2
	v_add_u32_e32 v3, v5, v3
	v_cmp_ne_u32_e32 vcc, v4, v3
	s_and_saveexec_b64 s[2:3], vcc
	s_xor_b64 s[10:11], exec, s[2:3]
	s_cbranch_execz .LBB0_1884
	s_waitcnt lgkmcnt(0)
	v_mov_b32_e32 v1, 0x2000
	global_load_dword v1, v1, s[8:9] offset:1024 sc1
	s_add_u32 s16, s8, 0x2400
	s_addc_u32 s17, s9, 0
	s_waitcnt vmcnt(0)
	v_cmp_eq_u32_e32 vcc, v1, v2
	s_and_saveexec_b64 s[14:15], vcc
	s_cbranch_execz .LBB0_1883
	s_mov_b32 s2, 1
	s_mov_b64 s[18:19], 0
	v_mov_b32_e32 v1, 0
	s_branch .LBB0_1874

; __device__ __forceinline__ unsigned xb_ld(unsigned* p)              { return __hip_atomic_load(p, __ATOMIC_RELAXED, __HIP_MEMORY_SCOPE_AGENT); }
; __device__ __forceinline__ unsigned xb_add(unsigned* p, unsigned v) { return __hip_atomic_fetch_add(p, v, __ATOMIC_RELAXED, __HIP_MEMORY_SCOPE_AGENT); }
; #define XB_SPIN(cond, bar) do { unsigned _sp = 0; while (cond) { __builtin_amdgcn_s_sleep(1); \
;     if ((++_sp & 255u) == 0u) { if (xb_ld(&(bar)[XB_TMO])) break; if (_sp > XB_SPIN_CAP) { atomicAdd(&(bar)[XB_TMO], 1u); break; } } } } while (0)
; __device__ __forceinline__ void xcd_barrier(const XcdBarrier& b) {
;     ...
;         if (old + 1u == (gen + 1u) * nloc) {
;             __builtin_amdgcn_fence(__ATOMIC_RELEASE, "agent");
;             asm volatile("s_waitcnt vmcnt(0)" ::: "memory");
;             const unsigned og = xb_add(&bar[XB_TOP], 1u);
;             const unsigned tg = og / nx;
;             if (og + 1u == (tg + 1u) * nx) xb_add(&bar[XB_TOPGEN], 1u);
;             else XB_SPIN(xb_ld(&bar[XB_TOPGEN]) == tg, bar);
;             __builtin_amdgcn_fence(__ATOMIC_ACQUIRE, "agent");
;             xb_add(&bar[XB_XGEN(b.x)], 1u);
;             asm volatile("s_waitcnt vmcnt(0)" ::: "memory");
;         } else {
;             XB_SPIN(xb_ld(&bar[XB_XGEN(b.x)]) == gen, bar);
;             __builtin_amdgcn_fence(__ATOMIC_ACQUIRE, "agent");
;             asm volatile("s_waitcnt vmcnt(0)" ::: "memory");
;         }
.LBB0_1883:
	s_or_b64 exec, exec, s[14:15]
	s_waitcnt vmcnt(0)
.LBB0_1884:
	s_andn2_saveexec_b64 s[2:3], s[10:11]
	s_cbranch_execz .LBB0_1904
	s_mov_b64 s[10:11], exec
	buffer_wbl2 sc1
	s_waitcnt lgkmcnt(0)
	s_waitcnt vmcnt(0)
	v_mbcnt_lo_u32_b32 v2, s10, 0
	v_mbcnt_hi_u32_b32 v2, s11, v2
	v_cmp_eq_u32_e32 vcc, 0, v2
	s_and_saveexec_b64 s[14:15], vcc
	s_cbranch_execz .LBB0_1887
	s_bcnt1_i32_b64 s2, s[10:11]
	v_mov_b32_e32 v3, 0x3000
	v_mov_b32_e32 v4, s2
	global_atomic_add v3, v3, v4, s[90:91] offset:1024 sc0

; __device__ __forceinline__ unsigned xb_add(unsigned* p, unsigned v) { return __hip_atomic_fetch_add(p, v, __ATOMIC_RELAXED, __HIP_MEMORY_SCOPE_AGENT); }
; __device__ __forceinline__ void xcd_barrier(const XcdBarrier& b) {
;     ...
;             __builtin_amdgcn_fence(__ATOMIC_ACQUIRE, "agent");
;             xb_add(&bar[XB_XGEN(b.x)], 1u);
;             asm volatile("s_waitcnt vmcnt(0)" ::: "memory");
.LBB0_1901:
	s_or_b64 exec, exec, s[10:11]
	s_mov_b64 s[10:11], exec
	v_mbcnt_lo_u32_b32 v1, s10, 0
	v_mbcnt_hi_u32_b32 v1, s11, v1
	v_cmp_eq_u32_e32 vcc, 0, v1
	s_waitcnt vmcnt(0)
	s_and_saveexec_b64 s[14:15], vcc
	s_cbranch_execz .LBB0_1903
	s_bcnt1_i32_b64 s2, s[10:11]
	v_mov_b32_e32 v1, 0x2000
	v_mov_b32_e32 v2, s2
	global_atomic_add v1, v2, s[8:9] offset:1024
